# baseline (speedup 1.0000x reference)
.Lq2_nd0_1:
	v_mfma_scale_f32_32x32x64_f8f6f4 v[18:33], v[66:73], v[146:153], 0, v203, v203 op_sel_hi:[0,0,0]
	v_exp_f32_e64 v2, -v2
	v_exp_f32_e64 v3, -v3
	v_exp_f32_e64 v4, -v4
	v_exp_f32_e64 v5, -v5
	s_waitcnt lgkmcnt(0)
	v_add_co_u32_e64 v200, s[42:43], v200, v200
	v_add_co_u32_e64 v200, s[48:49], v200, v200
	v_add_co_u32_e64 v200, s[50:51], v200, v200
	v_add_co_u32_e64 v200, s[56:57], v200, v200
	v_add_f32_e32 v2, v2, v162
	v_add_f32_e32 v3, v3, v163
	v_add_f32_e32 v4, v4, v164
	v_add_f32_e32 v5, v5, v165
	s_mov_b64 exec, s[42:43]
	v_mul_f32_e32 v204, v204, v2
	s_mov_b64 exec, s[48:49]
	v_mul_f32_e32 v205, v205, v3
	s_mov_b64 exec, s[50:51]
	v_mul_f32_e32 v206, v206, v4
	s_mov_b64 exec, s[56:57]
	v_mul_f32_e32 v207, v207, v5
	s_mov_b64 exec, -1
	s_nop 1
	v_mfma_scale_f32_32x32x64_f8f6f4 v[18:33], v[74:81], v[154:161], v[18:33], v203, v203 op_sel_hi:[0,0,0]
	v_exp_f32_e64 v6, -v6
	v_exp_f32_e64 v7, -v7
	v_exp_f32_e64 v8, -v8
	v_exp_f32_e64 v9, -v9
	v_add_co_u32_e64 v200, s[42:43], v200, v200
	v_add_co_u32_e64 v200, s[48:49], v200, v200
	v_add_co_u32_e64 v200, s[50:51], v200, v200
	v_add_co_u32_e64 v200, s[56:57], v200, v200
	v_add_f32_e32 v6, v6, v166
	v_add_f32_e32 v7, v7, v167
	v_add_f32_e32 v8, v8, v168
	v_add_f32_e32 v9, v9, v169
	s_mov_b64 exec, s[42:43]
	v_mul_f32_e32 v208, v208, v6
	s_mov_b64 exec, s[48:49]
	v_mul_f32_e32 v209, v209, v7
	s_mov_b64 exec, s[50:51]
	v_mul_f32_e32 v210, v210, v8
	s_mov_b64 exec, s[56:57]
	v_mul_f32_e32 v211, v211, v9
	s_mov_b64 exec, -1
	s_nop 1
	v_mfma_scale_f32_32x32x64_f8f6f4 v[18:33], v[82:89], v[138:145], v[18:33], v203, v203 op_sel_hi:[0,0,0]
	v_exp_f32_e64 v10, -v10
	v_exp_f32_e64 v11, -v11
	v_exp_f32_e64 v12, -v12
	v_exp_f32_e64 v13, -v13
	v_add_co_u32_e64 v200, s[42:43], v200, v200
	v_add_co_u32_e64 v200, s[48:49], v200, v200
	v_add_co_u32_e64 v200, s[50:51], v200, v200
	v_add_co_u32_e64 v200, s[56:57], v200, v200
	v_add_f32_e32 v10, v10, v170
	v_add_f32_e32 v11, v11, v171
	v_add_f32_e32 v12, v12, v172
	v_add_f32_e32 v13, v13, v173
	s_mov_b64 exec, s[42:43]
	v_mul_f32_e32 v212, v212, v10
	s_mov_b64 exec, s[48:49]
	v_mul_f32_e32 v213, v213, v11
	s_mov_b64 exec, s[50:51]
	v_mul_f32_e32 v214, v214, v12
	s_mov_b64 exec, s[56:57]
	v_mul_f32_e32 v215, v215, v13
	s_mov_b64 exec, -1
	s_nop 1
	v_mfma_scale_f32_32x32x64_f8f6f4 v[18:33], v[90:97], v[130:137], v[18:33], v203, v203 op_sel_hi:[0,0,0]
	v_exp_f32_e64 v14, -v14
	v_exp_f32_e64 v15, -v15
	v_exp_f32_e64 v16, -v16
	v_exp_f32_e64 v17, -v17
	v_add_co_u32_e64 v200, s[42:43], v200, v200
	v_add_co_u32_e64 v200, s[48:49], v200, v200
	v_add_co_u32_e64 v200, s[50:51], v200, v200
	v_add_co_u32_e64 v200, s[56:57], v200, v200
	v_add_f32_e32 v14, v14, v174
	v_add_f32_e32 v15, v15, v175
	v_add_f32_e32 v16, v16, v176
	v_add_f32_e32 v17, v17, v177
	s_mov_b64 exec, s[42:43]
	v_mul_f32_e32 v216, v216, v14
	s_mov_b64 exec, s[48:49]
	v_mul_f32_e32 v217, v217, v15
	s_mov_b64 exec, s[50:51]
	v_mul_f32_e32 v218, v218, v16
	s_mov_b64 exec, s[56:57]
	v_mul_f32_e32 v219, v219, v17
	s_mov_b64 exec, -1
	s_nop 1
	s_cmp_lg_u32 s55, s40
	s_cbranch_scc1 .Lq2_nd1_1
	s_nop 15
	s_nop 7
	v_cndmask_b32_e64 v18, v18, v199, s[0:1]
	v_cndmask_b32_e64 v19, v19, v199, s[2:3]
	v_cndmask_b32_e64 v20, v20, v199, s[4:5]
	v_cndmask_b32_e64 v21, v21, v199, s[6:7]
	v_cndmask_b32_e64 v22, v22, v199, s[8:9]
	v_cndmask_b32_e64 v23, v23, v199, s[10:11]
	v_cndmask_b32_e64 v24, v24, v199, s[12:13]
	v_cndmask_b32_e64 v25, v25, v199, s[14:15]
	v_cndmask_b32_e64 v26, v26, v199, s[16:17]
	v_cndmask_b32_e64 v27, v27, v199, s[18:19]
	v_cndmask_b32_e64 v28, v28, v199, s[20:21]
	v_cndmask_b32_e64 v29, v29, v199, s[22:23]
	v_cndmask_b32_e64 v30, v30, v199, s[24:25]
	v_cndmask_b32_e64 v31, v31, v199, s[26:27]
	v_cndmask_b32_e64 v32, v32, v199, s[28:29]
	v_cndmask_b32_e64 v33, v33, v199, s[30:31]
.Lq2_nd1_1:
	s_nop 3
	s_waitcnt vmcnt(6)
	v_mfma_scale_f32_32x32x64_f8f6f4 v[2:17], v[34:41], v[106:113], 0, v203, v203 op_sel_hi:[0,0,0]
	v_exp_f32_e64 v18, -v18
	v_exp_f32_e64 v19, -v19
	v_exp_f32_e64 v20, -v20
	v_exp_f32_e64 v21, -v21
	v_add_co_u32_e64 v200, s[42:43], v200, v200
	v_add_co_u32_e64 v200, s[48:49], v200, v200
	v_add_co_u32_e64 v200, s[50:51], v200, v200
	v_add_co_u32_e64 v200, s[56:57], v200, v200
	v_add_f32_e32 v18, v18, v178
	v_add_f32_e32 v19, v19, v179
	v_add_f32_e32 v20, v20, v180
	v_add_f32_e32 v21, v21, v181
	s_mov_b64 exec, s[42:43]
	v_mul_f32_e32 v220, v220, v18
	s_mov_b64 exec, s[48:49]
	v_mul_f32_e32 v221, v221, v19
	s_mov_b64 exec, s[50:51]
	v_mul_f32_e32 v222, v222, v20
	s_mov_b64 exec, s[56:57]
	v_mul_f32_e32 v223, v223, v21
	s_mov_b64 exec, -1
	s_nop 1
	s_waitcnt vmcnt(4)
	v_mfma_scale_f32_32x32x64_f8f6f4 v[2:17], v[42:49], v[122:129], v[2:17], v203, v203 op_sel_hi:[0,0,0]
	v_exp_f32_e64 v22, -v22
	v_exp_f32_e64 v23, -v23
	v_exp_f32_e64 v24, -v24
	v_exp_f32_e64 v25, -v25
	v_add_co_u32_e64 v200, s[42:43], v200, v200
	v_add_co_u32_e64 v200, s[48:49], v200, v200
	v_add_co_u32_e64 v200, s[50:51], v200, v200
	v_add_co_u32_e64 v200, s[56:57], v200, v200
	v_add_f32_e32 v22, v22, v182
	v_add_f32_e32 v23, v23, v183
	v_add_f32_e32 v24, v24, v184
	v_add_f32_e32 v25, v25, v185
	s_mov_b64 exec, s[42:43]
	v_mul_f32_e32 v224, v224, v22
	s_mov_b64 exec, s[48:49]
	v_mul_f32_e32 v225, v225, v23
	s_mov_b64 exec, s[50:51]
	v_mul_f32_e32 v226, v226, v24
	s_mov_b64 exec, s[56:57]
	v_mul_f32_e32 v227, v227, v25
	s_mov_b64 exec, -1
	s_nop 1
	s_waitcnt vmcnt(2)
	v_mfma_scale_f32_32x32x64_f8f6f4 v[2:17], v[50:57], v[114:121], v[2:17], v203, v203 op_sel_hi:[0,0,0]
	v_exp_f32_e64 v26, -v26
	v_exp_f32_e64 v27, -v27
	v_exp_f32_e64 v28, -v28
	v_exp_f32_e64 v29, -v29
	v_add_co_u32_e64 v200, s[42:43], v200, v200
	v_add_co_u32_e64 v200, s[48:49], v200, v200
	v_add_co_u32_e64 v200, s[50:51], v200, v200
	v_add_co_u32_e64 v200, s[56:57], v200, v200
	v_add_f32_e32 v26, v26, v186
	v_add_f32_e32 v27, v27, v187
	v_add_f32_e32 v28, v28, v188
	v_add_f32_e32 v29, v29, v189
	s_mov_b64 exec, s[42:43]
	v_mul_f32_e32 v228, v228, v26
	s_mov_b64 exec, s[48:49]
	v_mul_f32_e32 v229, v229, v27
	s_mov_b64 exec, s[50:51]
	v_mul_f32_e32 v230, v230, v28
	s_mov_b64 exec, s[56:57]
	v_mul_f32_e32 v231, v231, v29
	s_mov_b64 exec, -1
	s_nop 1
	s_waitcnt vmcnt(0)
	v_mfma_scale_f32_32x32x64_f8f6f4 v[2:17], v[58:65], v[98:105], v[2:17], v203, v203 op_sel_hi:[0,0,0]
	v_exp_f32_e64 v30, -v30
	v_exp_f32_e64 v31, -v31
	v_exp_f32_e64 v32, -v32
	v_exp_f32_e64 v33, -v33
	v_add_co_u32_e64 v200, s[42:43], v200, v200
	v_add_co_u32_e64 v200, s[48:49], v200, v200
	v_add_co_u32_e64 v200, s[50:51], v200, v200
	v_add_co_u32_e64 v200, s[56:57], v200, v200
	v_add_f32_e32 v30, v30, v190
	v_add_f32_e32 v31, v31, v191
	v_add_f32_e32 v32, v32, v192
	v_add_f32_e32 v33, v33, v193
	s_mov_b64 exec, s[42:43]
	v_mul_f32_e32 v232, v232, v30
	s_mov_b64 exec, s[48:49]
	v_mul_f32_e32 v233, v233, v31
	s_mov_b64 exec, s[50:51]
	v_mul_f32_e32 v234, v234, v32
	s_mov_b64 exec, s[56:57]
	v_mul_f32_e32 v235, v235, v33
	s_mov_b64 exec, -1
	s_nop 1
	s_lshl_b32 s34, s39, 2
	s_add_i32 s34, s34, 2
	s_add_i32 s34, s34, s35
	s_and_b32 s41, s34, 15
	s_add_i32 s54, s34, 1
	s_and_b32 s54, s54, 15
	s_lshl_b32 s55, s41, 8
	s_lshl_b32 s38, s52, 12
	s_add_i32 s55, s55, s38
	v_lshl_add_u32 v236, v194, 2, s55
	ds_read_b32 v200, v236
	s_lshl_b32 s34, s54, 3
	s_add_i32 s34, s34, s52
	s_lshl_b32 s34, s34, 13
	s_add_i32 s34, s34, s53
	buffer_load_dwordx4 v[146:149], v195, s[44:47], s34 offen
	s_or_b32 s42, s34, 0x400
	buffer_load_dwordx4 v[150:153], v195, s[44:47], s42 offen
	s_or_b32 s43, s34, 0x800
	buffer_load_dwordx4 v[154:157], v195, s[44:47], s43 offen
	s_or_b32 s42, s34, 0xc00
	buffer_load_dwordx4 v[158:161], v195, s[44:47], s42 offen
	s_or_b32 s43, s34, 0x1000
	buffer_load_dwordx4 v[138:141], v195, s[44:47], s43 offen
	s_or_b32 s42, s34, 0x1400
	buffer_load_dwordx4 v[142:145], v195, s[44:47], s42 offen
	s_or_b32 s43, s34, 0x1800
	buffer_load_dwordx4 v[130:133], v195, s[44:47], s43 offen
	s_or_b32 s42, s34, 0x1c00
	buffer_load_dwordx4 v[134:137], v195, s[44:47], s42 offen
	s_lshl_b32 s55, s41, 3
	s_add_i32 s55, s55, s52
	s_cmp_lg_u32 s55, s33
	s_cbranch_scc1 .Lq2_nd0_2
	v_cndmask_b32_e64 v2, v2, v198, s[0:1]
	v_cndmask_b32_e64 v3, v3, v198, s[2:3]
	v_cndmask_b32_e64 v4, v4, v198, s[4:5]
	v_cndmask_b32_e64 v5, v5, v198, s[6:7]
	v_cndmask_b32_e64 v6, v6, v198, s[8:9]
	v_cndmask_b32_e64 v7, v7, v198, s[10:11]
	v_cndmask_b32_e64 v8, v8, v198, s[12:13]
	v_cndmask_b32_e64 v9, v9, v198, s[14:15]
	v_cndmask_b32_e64 v10, v10, v198, s[16:17]
	v_cndmask_b32_e64 v11, v11, v198, s[18:19]
	v_cndmask_b32_e64 v12, v12, v198, s[20:21]
	v_cndmask_b32_e64 v13, v13, v198, s[22:23]
	v_cndmask_b32_e64 v14, v14, v198, s[24:25]
	v_cndmask_b32_e64 v15, v15, v198, s[26:27]
	v_cndmask_b32_e64 v16, v16, v198, s[28:29]
	v_cndmask_b32_e64 v17, v17, v198, s[30:31]
.Lq2_nd0_2:
	v_mfma_scale_f32_32x32x64_f8f6f4 v[18:33], v[66:73], v[106:113], 0, v203, v203 op_sel_hi:[0,0,0]
	v_exp_f32_e64 v2, -v2
	v_exp_f32_e64 v3, -v3
	v_exp_f32_e64 v4, -v4
	v_exp_f32_e64 v5, -v5
	s_waitcnt lgkmcnt(0)
	v_add_co_u32_e64 v200, s[42:43], v200, v200
	v_add_co_u32_e64 v200, s[48:49], v200, v200
	v_add_co_u32_e64 v200, s[50:51], v200, v200
	v_add_co_u32_e64 v200, s[56:57], v200, v200
	v_add_f32_e32 v2, v2, v162
	v_add_f32_e32 v3, v3, v163
	v_add_f32_e32 v4, v4, v164
	v_add_f32_e32 v5, v5, v165
	s_mov_b64 exec, s[42:43]
	v_mul_f32_e32 v204, v204, v2
	s_mov_b64 exec, s[48:49]
	v_mul_f32_e32 v205, v205, v3
	s_mov_b64 exec, s[50:51]
	v_mul_f32_e32 v206, v206, v4
	s_mov_b64 exec, s[56:57]
	v_mul_f32_e32 v207, v207, v5
	s_mov_b64 exec, -1
	s_nop 1
	v_mfma_scale_f32_32x32x64_f8f6f4 v[18:33], v[74:81], v[122:129], v[18:33], v203, v203 op_sel_hi:[0,0,0]
	v_exp_f32_e64 v6, -v6
	v_exp_f32_e64 v7, -v7
	v_exp_f32_e64 v8, -v8
	v_exp_f32_e64 v9, -v9
	v_add_co_u32_e64 v200, s[42:43], v200, v200
	v_add_co_u32_e64 v200, s[48:49], v200, v200
	v_add_co_u32_e64 v200, s[50:51], v200, v200
	v_add_co_u32_e64 v200, s[56:57], v200, v200
	v_add_f32_e32 v6, v6, v166
	v_add_f32_e32 v7, v7, v167
	v_add_f32_e32 v8, v8, v168
	v_add_f32_e32 v9, v9, v169
	s_mov_b64 exec, s[42:43]
	v_mul_f32_e32 v208, v208, v6
	s_mov_b64 exec, s[48:49]
	v_mul_f32_e32 v209, v209, v7
	s_mov_b64 exec, s[50:51]
	v_mul_f32_e32 v210, v210, v8
	s_mov_b64 exec, s[56:57]
	v_mul_f32_e32 v211, v211, v9
	s_mov_b64 exec, -1
	s_nop 1
	v_mfma_scale_f32_32x32x64_f8f6f4 v[18:33], v[82:89], v[114:121], v[18:33], v203, v203 op_sel_hi:[0,0,0]
	v_exp_f32_e64 v10, -v10
	v_exp_f32_e64 v11, -v11
	v_exp_f32_e64 v12, -v12
	v_exp_f32_e64 v13, -v13
	v_add_co_u32_e64 v200, s[42:43], v200, v200
	v_add_co_u32_e64 v200, s[48:49], v200, v200
	v_add_co_u32_e64 v200, s[50:51], v200, v200
	v_add_co_u32_e64 v200, s[56:57], v200, v200
	v_add_f32_e32 v10, v10, v170
	v_add_f32_e32 v11, v11, v171
	v_add_f32_e32 v12, v12, v172
	v_add_f32_e32 v13, v13, v173
	s_mov_b64 exec, s[42:43]
	v_mul_f32_e32 v212, v212, v10
	s_mov_b64 exec, s[48:49]
	v_mul_f32_e32 v213, v213, v11
	s_mov_b64 exec, s[50:51]
	v_mul_f32_e32 v214, v214, v12
	s_mov_b64 exec, s[56:57]
	v_mul_f32_e32 v215, v215, v13
	s_mov_b64 exec, -1
	s_nop 1
	v_mfma_scale_f32_32x32x64_f8f6f4 v[18:33], v[90:97], v[98:105], v[18:33], v203, v203 op_sel_hi:[0,0,0]
	v_exp_f32_e64 v14, -v14
	v_exp_f32_e64 v15, -v15
	v_exp_f32_e64 v16, -v16
	v_exp_f32_e64 v17, -v17
	v_add_co_u32_e64 v200, s[42:43], v200, v200
	v_add_co_u32_e64 v200, s[48:49], v200, v200
	v_add_co_u32_e64 v200, s[50:51], v200, v200
	v_add_co_u32_e64 v200, s[56:57], v200, v200
	v_add_f32_e32 v14, v14, v174
	v_add_f32_e32 v15, v15, v175
	v_add_f32_e32 v16, v16, v176
	v_add_f32_e32 v17, v17, v177
	s_mov_b64 exec, s[42:43]
	v_mul_f32_e32 v216, v216, v14
	s_mov_b64 exec, s[48:49]
	v_mul_f32_e32 v217, v217, v15
	s_mov_b64 exec, s[50:51]
	v_mul_f32_e32 v218, v218, v16
	s_mov_b64 exec, s[56:57]
	v_mul_f32_e32 v219, v219, v17
	s_mov_b64 exec, -1
	s_nop 1
	s_cmp_lg_u32 s55, s40
	s_cbranch_scc1 .Lq2_nd1_2
	s_nop 15
	s_nop 7
	v_cndmask_b32_e64 v18, v18, v199, s[0:1]
	v_cndmask_b32_e64 v19, v19, v199, s[2:3]
	v_cndmask_b32_e64 v20, v20, v199, s[4:5]
	v_cndmask_b32_e64 v21, v21, v199, s[6:7]
	v_cndmask_b32_e64 v22, v22, v199, s[8:9]
	v_cndmask_b32_e64 v23, v23, v199, s[10:11]
	v_cndmask_b32_e64 v24, v24, v199, s[12:13]
	v_cndmask_b32_e64 v25, v25, v199, s[14:15]
	v_cndmask_b32_e64 v26, v26, v199, s[16:17]
	v_cndmask_b32_e64 v27, v27, v199, s[18:19]
	v_cndmask_b32_e64 v28, v28, v199, s[20:21]
	v_cndmask_b32_e64 v29, v29, v199, s[22:23]
	v_cndmask_b32_e64 v30, v30, v199, s[24:25]
	v_cndmask_b32_e64 v31, v31, v199, s[26:27]
	v_cndmask_b32_e64 v32, v32, v199, s[28:29]
	v_cndmask_b32_e64 v33, v33, v199, s[30:31]
.Lq2_nd1_2:
	s_nop 3
	s_waitcnt vmcnt(6)
	v_mfma_scale_f32_32x32x64_f8f6f4 v[2:17], v[34:41], v[146:153], 0, v203, v203 op_sel_hi:[0,0,0]
	v_exp_f32_e64 v18, -v18
	v_exp_f32_e64 v19, -v19
	v_exp_f32_e64 v20, -v20
	v_exp_f32_e64 v21, -v21
	v_add_co_u32_e64 v200, s[42:43], v200, v200
	v_add_co_u32_e64 v200, s[48:49], v200, v200
	v_add_co_u32_e64 v200, s[50:51], v200, v200
	v_add_co_u32_e64 v200, s[56:57], v200, v200
	v_add_f32_e32 v18, v18, v178
	v_add_f32_e32 v19, v19, v179
	v_add_f32_e32 v20, v20, v180
	v_add_f32_e32 v21, v21, v181
	s_mov_b64 exec, s[42:43]
	v_mul_f32_e32 v220, v220, v18
	s_mov_b64 exec, s[48:49]
	v_mul_f32_e32 v221, v221, v19
	s_mov_b64 exec, s[50:51]
	v_mul_f32_e32 v222, v222, v20
	s_mov_b64 exec, s[56:57]
	v_mul_f32_e32 v223, v223, v21
	s_mov_b64 exec, -1
	s_nop 1
	s_waitcnt vmcnt(4)
	v_mfma_scale_f32_32x32x64_f8f6f4 v[2:17], v[42:49], v[154:161], v[2:17], v203, v203 op_sel_hi:[0,0,0]
	v_exp_f32_e64 v22, -v22
	v_exp_f32_e64 v23, -v23
	v_exp_f32_e64 v24, -v24
	v_exp_f32_e64 v25, -v25
	v_add_co_u32_e64 v200, s[42:43], v200, v200
	v_add_co_u32_e64 v200, s[48:49], v200, v200
	v_add_co_u32_e64 v200, s[50:51], v200, v200
	v_add_co_u32_e64 v200, s[56:57], v200, v200
	v_add_f32_e32 v22, v22, v182
	v_add_f32_e32 v23, v23, v183
	v_add_f32_e32 v24, v24, v184
	v_add_f32_e32 v25, v25, v185
	s_mov_b64 exec, s[42:43]
	v_mul_f32_e32 v224, v224, v22
	s_mov_b64 exec, s[48:49]
	v_mul_f32_e32 v225, v225, v23
	s_mov_b64 exec, s[50:51]
	v_mul_f32_e32 v226, v226, v24
	s_mov_b64 exec, s[56:57]
	v_mul_f32_e32 v227, v227, v25
	s_mov_b64 exec, -1
	s_nop 1
	s_waitcnt vmcnt(2)
	v_mfma_scale_f32_32x32x64_f8f6f4 v[2:17], v[50:57], v[138:145], v[2:17], v203, v203 op_sel_hi:[0,0,0]
	v_exp_f32_e64 v26, -v26
	v_exp_f32_e64 v27, -v27
	v_exp_f32_e64 v28, -v28
	v_exp_f32_e64 v29, -v29
	v_add_co_u32_e64 v200, s[42:43], v200, v200
	v_add_co_u32_e64 v200, s[48:49], v200, v200
	v_add_co_u32_e64 v200, s[50:51], v200, v200
	v_add_co_u32_e64 v200, s[56:57], v200, v200
	v_add_f32_e32 v26, v26, v186
	v_add_f32_e32 v27, v27, v187
	v_add_f32_e32 v28, v28, v188
	v_add_f32_e32 v29, v29, v189
	s_mov_b64 exec, s[42:43]
	v_mul_f32_e32 v228, v228, v26
	s_mov_b64 exec, s[48:49]
	v_mul_f32_e32 v229, v229, v27
	s_mov_b64 exec, s[50:51]
	v_mul_f32_e32 v230, v230, v28
	s_mov_b64 exec, s[56:57]
	v_mul_f32_e32 v231, v231, v29
	s_mov_b64 exec, -1
	s_nop 1
	s_waitcnt vmcnt(0)
	v_mfma_scale_f32_32x32x64_f8f6f4 v[2:17], v[58:65], v[130:137], v[2:17], v203, v203 op_sel_hi:[0,0,0]
	v_exp_f32_e64 v30, -v30
	v_exp_f32_e64 v31, -v31
	v_exp_f32_e64 v32, -v32
	v_exp_f32_e64 v33, -v33
	v_add_co_u32_e64 v200, s[42:43], v200, v200
	v_add_co_u32_e64 v200, s[48:49], v200, v200
	v_add_co_u32_e64 v200, s[50:51], v200, v200
	v_add_co_u32_e64 v200, s[56:57], v200, v200
	v_add_f32_e32 v30, v30, v190
	v_add_f32_e32 v31, v31, v191
	v_add_f32_e32 v32, v32, v192
	v_add_f32_e32 v33, v33, v193
	s_mov_b64 exec, s[42:43]
	v_mul_f32_e32 v232, v232, v30
	s_mov_b64 exec, s[48:49]
	v_mul_f32_e32 v233, v233, v31
	s_mov_b64 exec, s[50:51]
	v_mul_f32_e32 v234, v234, v32
	s_mov_b64 exec, s[56:57]
	v_mul_f32_e32 v235, v235, v33
	s_mov_b64 exec, -1
	s_nop 1
	s_lshl_b32 s34, s39, 2
	s_add_i32 s34, s34, 3
	s_add_i32 s34, s34, s35
	s_and_b32 s41, s34, 15
	s_add_i32 s54, s34, 1
	s_and_b32 s54, s54, 15
	s_lshl_b32 s55, s41, 8
	s_lshl_b32 s38, s52, 12
	s_add_i32 s55, s55, s38
	v_lshl_add_u32 v236, v194, 2, s55
	ds_read_b32 v200, v236
	s_lshl_b32 s34, s54, 3
	s_add_i32 s34, s34, s52
	s_lshl_b32 s34, s34, 13
	s_add_i32 s34, s34, s53
	buffer_load_dwordx4 v[106:109], v195, s[44:47], s34 offen
	s_or_b32 s42, s34, 0x400
	buffer_load_dwordx4 v[110:113], v195, s[44:47], s42 offen
	s_or_b32 s43, s34, 0x800
	buffer_load_dwordx4 v[122:125], v195, s[44:47], s43 offen
	s_or_b32 s42, s34, 0xc00
	buffer_load_dwordx4 v[126:129], v195, s[44:47], s42 offen
	s_or_b32 s43, s34, 0x1000
	buffer_load_dwordx4 v[114:117], v195, s[44:47], s43 offen
	s_or_b32 s42, s34, 0x1400
	buffer_load_dwordx4 v[118:121], v195, s[44:47], s42 offen
	s_or_b32 s43, s34, 0x1800
	buffer_load_dwordx4 v[98:101], v195, s[44:47], s43 offen
	s_or_b32 s42, s34, 0x1c00
	buffer_load_dwordx4 v[102:105], v195, s[44:47], s42 offen
	s_lshl_b32 s55, s41, 3
	s_add_i32 s55, s55, s52
	s_cmp_lg_u32 s55, s33
	s_cbranch_scc1 .Lq2_nd0_3
	v_cndmask_b32_e64 v2, v2, v198, s[0:1]
	v_cndmask_b32_e64 v3, v3, v198, s[2:3]
	v_cndmask_b32_e64 v4, v4, v198, s[4:5]
	v_cndmask_b32_e64 v5, v5, v198, s[6:7]
	v_cndmask_b32_e64 v6, v6, v198, s[8:9]
	v_cndmask_b32_e64 v7, v7, v198, s[10:11]
	v_cndmask_b32_e64 v8, v8, v198, s[12:13]
	v_cndmask_b32_e64 v9, v9, v198, s[14:15]
	v_cndmask_b32_e64 v10, v10, v198, s[16:17]
	v_cndmask_b32_e64 v11, v11, v198, s[18:19]
	v_cndmask_b32_e64 v12, v12, v198, s[20:21]
	v_cndmask_b32_e64 v13, v13, v198, s[22:23]
	v_cndmask_b32_e64 v14, v14, v198, s[24:25]
	v_cndmask_b32_e64 v15, v15, v198, s[26:27]
	v_cndmask_b32_e64 v16, v16, v198, s[28:29]
	v_cndmask_b32_e64 v17, v17, v198, s[30:31]
.Lq2_nd0_3:
	v_mfma_scale_f32_32x32x64_f8f6f4 v[18:33], v[66:73], v[146:153], 0, v203, v203 op_sel_hi:[0,0,0]
	ds_read_b128 v[236:239], v202
	v_exp_f32_e64 v2, -v2
	v_exp_f32_e64 v3, -v3
	v_exp_f32_e64 v4, -v4
	v_exp_f32_e64 v5, -v5
	s_waitcnt lgkmcnt(1)
	v_add_co_u32_e64 v200, s[42:43], v200, v200
	v_add_co_u32_e64 v200, s[48:49], v200, v200
	v_add_co_u32_e64 v200, s[50:51], v200, v200
	v_add_co_u32_e64 v200, s[56:57], v200, v200
	v_add_f32_e32 v2, v2, v162
	v_add_f32_e32 v3, v3, v163
	v_add_f32_e32 v4, v4, v164
	v_add_f32_e32 v5, v5, v165
	s_mov_b64 exec, s[42:43]
	v_mul_f32_e32 v204, v204, v2
	s_mov_b64 exec, s[48:49]
	v_mul_f32_e32 v205, v205, v3
	s_mov_b64 exec, s[50:51]
	v_mul_f32_e32 v206, v206, v4
	s_mov_b64 exec, s[56:57]
	v_mul_f32_e32 v207, v207, v5
	s_mov_b64 exec, -1
	s_nop 1
	v_log_f32_e32 v2, v204
	v_log_f32_e32 v3, v205
	v_log_f32_e32 v4, v206
	v_log_f32_e32 v5, v207
	s_waitcnt lgkmcnt(0)
	v_fmac_f32_e32 v201, v2, v236
	v_fmac_f32_e32 v201, v3, v237
	v_fmac_f32_e32 v201, v4, v238
	v_fmac_f32_e32 v201, v5, v239
	v_mfma_scale_f32_32x32x64_f8f6f4 v[18:33], v[74:81], v[154:161], v[18:33], v203, v203 op_sel_hi:[0,0,0]
	ds_read_b128 v[236:239], v202 offset:16
	v_exp_f32_e64 v6, -v6
	v_exp_f32_e64 v7, -v7
	v_exp_f32_e64 v8, -v8
	v_exp_f32_e64 v9, -v9
	v_add_co_u32_e64 v200, s[42:43], v200, v200
	v_add_co_u32_e64 v200, s[48:49], v200, v200
	v_add_co_u32_e64 v200, s[50:51], v200, v200
	v_add_co_u32_e64 v200, s[56:57], v200, v200
	v_add_f32_e32 v6, v6, v166
	v_add_f32_e32 v7, v7, v167
	v_add_f32_e32 v8, v8, v168
	v_add_f32_e32 v9, v9, v169
	s_mov_b64 exec, s[42:43]
	v_mul_f32_e32 v208, v208, v6
	s_mov_b64 exec, s[48:49]
	v_mul_f32_e32 v209, v209, v7
	s_mov_b64 exec, s[50:51]
	v_mul_f32_e32 v210, v210, v8
	s_mov_b64 exec, s[56:57]
	v_mul_f32_e32 v211, v211, v9
	s_mov_b64 exec, -1
	s_nop 1
	v_log_f32_e32 v6, v208
	v_log_f32_e32 v7, v209
	v_log_f32_e32 v8, v210
	v_log_f32_e32 v9, v211
	s_waitcnt lgkmcnt(0)
	v_fmac_f32_e32 v201, v6, v236
	v_fmac_f32_e32 v201, v7, v237
	v_fmac_f32_e32 v201, v8, v238
	v_fmac_f32_e32 v201, v9, v239
	v_mfma_scale_f32_32x32x64_f8f6f4 v[18:33], v[82:89], v[138:145], v[18:33], v203, v203 op_sel_hi:[0,0,0]
	ds_read_b128 v[236:239], v202 offset:32
	v_exp_f32_e64 v10, -v10
	v_exp_f32_e64 v11, -v11
	v_exp_f32_e64 v12, -v12
	v_exp_f32_e64 v13, -v13
	v_add_co_u32_e64 v200, s[42:43], v200, v200
	v_add_co_u32_e64 v200, s[48:49], v200, v200
	v_add_co_u32_e64 v200, s[50:51], v200, v200
	v_add_co_u32_e64 v200, s[56:57], v200, v200
	v_add_f32_e32 v10, v10, v170
	v_add_f32_e32 v11, v11, v171
	v_add_f32_e32 v12, v12, v172
	v_add_f32_e32 v13, v13, v173
	s_mov_b64 exec, s[42:43]
	v_mul_f32_e32 v212, v212, v10
	s_mov_b64 exec, s[48:49]
	v_mul_f32_e32 v213, v213, v11
	s_mov_b64 exec, s[50:51]
	v_mul_f32_e32 v214, v214, v12
	s_mov_b64 exec, s[56:57]
	v_mul_f32_e32 v215, v215, v13
	s_mov_b64 exec, -1
	s_nop 1
	v_log_f32_e32 v10, v212
	v_log_f32_e32 v11, v213
	v_log_f32_e32 v12, v214
	v_log_f32_e32 v13, v215
	s_waitcnt lgkmcnt(0)
	v_fmac_f32_e32 v201, v10, v236
	v_fmac_f32_e32 v201, v11, v237
	v_fmac_f32_e32 v201, v12, v238
	v_fmac_f32_e32 v201, v13, v239
	v_mfma_scale_f32_32x32x64_f8f6f4 v[18:33], v[90:97], v[130:137], v[18:33], v203, v203 op_sel_hi:[0,0,0]
	ds_read_b128 v[236:239], v202 offset:48
	v_exp_f32_e64 v14, -v14
	v_exp_f32_e64 v15, -v15
	v_exp_f32_e64 v16, -v16
	v_exp_f32_e64 v17, -v17
	v_add_co_u32_e64 v200, s[42:43], v200, v200
	v_add_co_u32_e64 v200, s[48:49], v200, v200
	v_add_co_u32_e64 v200, s[50:51], v200, v200
	v_add_co_u32_e64 v200, s[56:57], v200, v200
	v_add_f32_e32 v14, v14, v174
	v_add_f32_e32 v15, v15, v175
	v_add_f32_e32 v16, v16, v176
	v_add_f32_e32 v17, v17, v177
	s_mov_b64 exec, s[42:43]
	v_mul_f32_e32 v216, v216, v14
	s_mov_b64 exec, s[48:49]
	v_mul_f32_e32 v217, v217, v15
	s_mov_b64 exec, s[50:51]
	v_mul_f32_e32 v218, v218, v16
	s_mov_b64 exec, s[56:57]
	v_mul_f32_e32 v219, v219, v17
	s_mov_b64 exec, -1
	s_nop 1
	v_log_f32_e32 v14, v216
	v_log_f32_e32 v15, v217
	v_log_f32_e32 v16, v218
	v_log_f32_e32 v17, v219
	s_waitcnt lgkmcnt(0)
	v_fmac_f32_e32 v201, v14, v236
	v_fmac_f32_e32 v201, v15, v237
	v_fmac_f32_e32 v201, v16, v238
	v_fmac_f32_e32 v201, v17, v239
	s_cmp_lg_u32 s55, s40
	s_cbranch_scc1 .Lq2_nd1_3
	s_nop 15
	s_nop 7
	v_cndmask_b32_e64 v18, v18, v199, s[0:1]
	v_cndmask_b32_e64 v19, v19, v199, s[2:3]
	v_cndmask_b32_e64 v20, v20, v199, s[4:5]
	v_cndmask_b32_e64 v21, v21, v199, s[6:7]
	v_cndmask_b32_e64 v22, v22, v199, s[8:9]
	v_cndmask_b32_e64 v23, v23, v199, s[10:11]
	v_cndmask_b32_e64 v24, v24, v199, s[12:13]
	v_cndmask_b32_e64 v25, v25, v199, s[14:15]
	v_cndmask_b32_e64 v26, v26, v199, s[16:17]
	v_cndmask_b32_e64 v27, v27, v199, s[18:19]
	v_cndmask_b32_e64 v28, v28, v199, s[20:21]
	v_cndmask_b32_e64 v29, v29, v199, s[22:23]
	v_cndmask_b32_e64 v30, v30, v199, s[24:25]
	v_cndmask_b32_e64 v31, v31, v199, s[26:27]
	v_cndmask_b32_e64 v32, v32, v199, s[28:29]
	v_cndmask_b32_e64 v33, v33, v199, s[30:31]
.Lq2_nd1_3:
	s_nop 3
	s_waitcnt vmcnt(6)
	v_mfma_scale_f32_32x32x64_f8f6f4 v[2:17], v[34:41], v[106:113], 0, v203, v203 op_sel_hi:[0,0,0]
	ds_read_b128 v[236:239], v202 offset:64
	v_exp_f32_e64 v18, -v18
	v_exp_f32_e64 v19, -v19
	v_exp_f32_e64 v20, -v20
	v_exp_f32_e64 v21, -v21
	v_add_co_u32_e64 v200, s[42:43], v200, v200
	v_add_co_u32_e64 v200, s[48:49], v200, v200
	v_add_co_u32_e64 v200, s[50:51], v200, v200
	v_add_co_u32_e64 v200, s[56:57], v200, v200
	v_add_f32_e32 v18, v18, v178
	v_add_f32_e32 v19, v19, v179
	v_add_f32_e32 v20, v20, v180
	v_add_f32_e32 v21, v21, v181
	s_mov_b64 exec, s[42:43]
	v_mul_f32_e32 v220, v220, v18
	s_mov_b64 exec, s[48:49]
	v_mul_f32_e32 v221, v221, v19
	s_mov_b64 exec, s[50:51]
	v_mul_f32_e32 v222, v222, v20
	s_mov_b64 exec, s[56:57]
	v_mul_f32_e32 v223, v223, v21
	s_mov_b64 exec, -1
	s_nop 1
	v_log_f32_e32 v18, v220
	v_log_f32_e32 v19, v221
	v_log_f32_e32 v20, v222
	v_log_f32_e32 v21, v223
	s_waitcnt lgkmcnt(0)
	v_fmac_f32_e32 v201, v18, v236
	v_fmac_f32_e32 v201, v19, v237
	v_fmac_f32_e32 v201, v20, v238
	v_fmac_f32_e32 v201, v21, v239
	s_waitcnt vmcnt(4)
	v_mfma_scale_f32_32x32x64_f8f6f4 v[2:17], v[42:49], v[122:129], v[2:17], v203, v203 op_sel_hi:[0,0,0]
	ds_read_b128 v[236:239], v202 offset:80
	v_exp_f32_e64 v22, -v22
	v_exp_f32_e64 v23, -v23
	v_exp_f32_e64 v24, -v24
	v_exp_f32_e64 v25, -v25
	v_add_co_u32_e64 v200, s[42:43], v200, v200
	v_add_co_u32_e64 v200, s[48:49], v200, v200
	v_add_co_u32_e64 v200, s[50:51], v200, v200
	v_add_co_u32_e64 v200, s[56:57], v200, v200
	v_add_f32_e32 v22, v22, v182
	v_add_f32_e32 v23, v23, v183
	v_add_f32_e32 v24, v24, v184
	v_add_f32_e32 v25, v25, v185
	s_mov_b64 exec, s[42:43]
	v_mul_f32_e32 v224, v224, v22
	s_mov_b64 exec, s[48:49]
	v_mul_f32_e32 v225, v225, v23
	s_mov_b64 exec, s[50:51]
	v_mul_f32_e32 v226, v226, v24
	s_mov_b64 exec, s[56:57]
	v_mul_f32_e32 v227, v227, v25
	s_mov_b64 exec, -1
	s_nop 1
	v_log_f32_e32 v22, v224
	v_log_f32_e32 v23, v225
	v_log_f32_e32 v24, v226
	v_log_f32_e32 v25, v227
	s_waitcnt lgkmcnt(0)
	v_fmac_f32_e32 v201, v22, v236
	v_fmac_f32_e32 v201, v23, v237
	v_fmac_f32_e32 v201, v24, v238
	v_fmac_f32_e32 v201, v25, v239
	s_waitcnt vmcnt(2)
	v_mfma_scale_f32_32x32x64_f8f6f4 v[2:17], v[50:57], v[114:121], v[2:17], v203, v203 op_sel_hi:[0,0,0]
	ds_read_b128 v[236:239], v202 offset:96
	v_exp_f32_e64 v26, -v26
	v_exp_f32_e64 v27, -v27
	v_exp_f32_e64 v28, -v28
	v_exp_f32_e64 v29, -v29
	v_add_co_u32_e64 v200, s[42:43], v200, v200
	v_add_co_u32_e64 v200, s[48:49], v200, v200
	v_add_co_u32_e64 v200, s[50:51], v200, v200
	v_add_co_u32_e64 v200, s[56:57], v200, v200
	v_add_f32_e32 v26, v26, v186
	v_add_f32_e32 v27, v27, v187
	v_add_f32_e32 v28, v28, v188
	v_add_f32_e32 v29, v29, v189
	s_mov_b64 exec, s[42:43]
	v_mul_f32_e32 v228, v228, v26
	s_mov_b64 exec, s[48:49]
	v_mul_f32_e32 v229, v229, v27
	s_mov_b64 exec, s[50:51]
	v_mul_f32_e32 v230, v230, v28
	s_mov_b64 exec, s[56:57]
	v_mul_f32_e32 v231, v231, v29
	s_mov_b64 exec, -1
	s_nop 1
	v_log_f32_e32 v26, v228
	v_log_f32_e32 v27, v229
	v_log_f32_e32 v28, v230
	v_log_f32_e32 v29, v231
	s_waitcnt lgkmcnt(0)
	v_fmac_f32_e32 v201, v26, v236
	v_fmac_f32_e32 v201, v27, v237
	v_fmac_f32_e32 v201, v28, v238
	v_fmac_f32_e32 v201, v29, v239
	s_waitcnt vmcnt(0)
	v_mfma_scale_f32_32x32x64_f8f6f4 v[2:17], v[58:65], v[98:105], v[2:17], v203, v203 op_sel_hi:[0,0,0]
	ds_read_b128 v[236:239], v202 offset:112
	v_exp_f32_e64 v30, -v30
	v_exp_f32_e64 v31, -v31
	v_exp_f32_e64 v32, -v32
	v_exp_f32_e64 v33, -v33
	v_add_co_u32_e64 v200, s[42:43], v200, v200
	v_add_co_u32_e64 v200, s[48:49], v200, v200
	v_add_co_u32_e64 v200, s[50:51], v200, v200
	v_add_co_u32_e64 v200, s[56:57], v200, v200
	v_add_f32_e32 v30, v30, v190
	v_add_f32_e32 v31, v31, v191
	v_add_f32_e32 v32, v32, v192
	v_add_f32_e32 v33, v33, v193
	s_mov_b64 exec, s[42:43]
	v_mul_f32_e32 v232, v232, v30
	s_mov_b64 exec, s[48:49]
	v_mul_f32_e32 v233, v233, v31
	s_mov_b64 exec, s[50:51]
	v_mul_f32_e32 v234, v234, v32
	s_mov_b64 exec, s[56:57]
	v_mul_f32_e32 v235, v235, v33
	s_mov_b64 exec, -1
	s_nop 1
	v_log_f32_e32 v30, v232
	v_log_f32_e32 v31, v233
	v_log_f32_e32 v32, v234
	v_log_f32_e32 v33, v235
	s_waitcnt lgkmcnt(0)
	v_fmac_f32_e32 v201, v30, v236
	v_fmac_f32_e32 v201, v31, v237
	v_fmac_f32_e32 v201, v32, v238
	v_fmac_f32_e32 v201, v33, v239
	s_add_i32 s39, s39, 1
	s_cmp_lt_u32 s39, 4
	s_cbranch_scc1 .Lq2_loop
